# bundle: P9 3-of-8 epilogue stores deferred into next unit's load slots; fp8 GEMM accumulator zeroing replaced by C=0 on first K-tile MFMAs (P8,P9); 20% of expert weight conversion moved into P3's idle
# speedup vs baseline: 1.0048x; 1.0042x over previous
; #define CV_LOAD(c) do { _Pragma("unroll") for (int nh = 0; nh < 2; ++nh) _Pragma("unroll") for (int q = 0; q < 4; ++q) { const float* p_ = (c).src + (size_t)(krow + 4 * q) * (c).N + 32 * nh + 8 * lg; \
;         v[(nh * 4 + q) * 2] = *(const f32x4*)p_; v[(nh * 4 + q) * 2 + 1] = *(const f32x4*)(p_ + 4); } } while (0)
; __device__ __forceinline__ CvItem cv_decode(const void* const* in, unsigned char* ws, int r) {
;     constexpr int I_EI = 32 * 16, I_EO = 8 * 32; CvItem c;
;     if (r < 65 * I_EI) { const int e = r / I_EI, q = r % I_EI, kb = 2 * ((q >> 1) / 16) + (q & 1), nb = (q >> 1) % 16, n0 = 64 * nb, j = n0 & 511, up = n0 >> 9;
;         const float* W = (e < 64) ? (const float*)in[20] + (size_t)e * DM * 1024 : (const float*)in[22];
;         c.src = W + (size_t)(64 * kb) * 1024 + n0; c.N = 1024; c.K = DM; c.scale = SC_WEI;
;         c.dst = ws + WS_WEI + (size_t)e * 1024 * DM + (size_t)((j >> 7) * 256 + up * 128 + (j & 127)) * DM + 64 * kb; }
;     else { r -= 65 * I_EI; const int e = r / I_EO, q = r % I_EO, kb = 2 * ((q >> 1) / 32) + (q & 1), nb = (q >> 1) % 32;
;         const float* W = (e < 64) ? (const float*)in[21] + (size_t)e * EH * DM : (const float*)in[23];
;         c.src = W + (size_t)(64 * kb) * DM + 64 * nb; c.N = DM; c.K = EH; c.scale = SC_WEO;
;         c.dst = ws + WS_WEO + (size_t)e * DM * EH + (size_t)(64 * nb) * EH + 64 * kb; }
;     return c;
; }
; __device__ __forceinline__ void p2_convert_experts(Ctx& F) {
;     const int gw = F.vcu * NWAVES + F.wave, NGW = F.G * NWAVES, lane = F.lane, li = lane & 15, lg = lane >> 4;
;     constexpr int NCV = 65 * (32 * 16 + 8 * 32);
;     int it = gw; CvItem cur; f32x4 v[16];
;     const int krow = 16 * (li >> 2) + (li & 3);
;     ...
;     if (it < NCV) { cur = cv_decode(F.in, F.ws, it); CV_LOAD(cur); }
;     while (it < NCV) {
; __global__ void __launch_bounds__(NWAVES * 64, 2) fwd_kernel(Args args) {
;     ...
;     if (IN(2)) {
;         if (F.vcu & 1) p2_convert_experts(F);
.LBB0_149:
	s_cmp_lt_i32 s86, 3
	s_cselect_b64 s[0:1], -1, 0
	s_cmp_gt_i32 s87, 2
	s_mov_b64 s[12:13], s[52:53]
	s_cselect_b64 s[4:5], -1, 0
	s_mov_b64 s[14:15], s[54:55]
	s_mov_b64 s[16:17], s[56:57]
	s_mov_b64 s[18:19], s[58:59]
	s_mov_b64 s[6:7], s[46:47]
	s_mov_b64 s[10:11], s[50:51]
	s_and_b64 s[0:1], s[0:1], s[4:5]
	v_writelane_b32 v253, s4, 41
	s_andn2_b64 vcc, exec, s[0:1]
	s_nop 0
	v_writelane_b32 v253, s5, 42
	v_writelane_b32 v253, s6, 43
	v_writelane_b32 v253, s7, 44
	v_writelane_b32 v253, s8, 45
	v_writelane_b32 v253, s9, 46
	v_writelane_b32 v253, s10, 47
	v_writelane_b32 v253, s11, 48
	v_writelane_b32 v253, s12, 49
	v_writelane_b32 v253, s13, 50
	v_writelane_b32 v253, s14, 51
	v_writelane_b32 v253, s15, 52
	v_writelane_b32 v253, s16, 53
	v_writelane_b32 v253, s17, 54
	v_writelane_b32 v253, s18, 55
	v_writelane_b32 v253, s19, 56
	s_cbranch_vccnz .LBB0_308
	s_and_b32 s3, s85, 1
	s_cmp_eq_u32 s3, 0
	s_cselect_b64 s[0:1], -1, 0
	s_cmp_eq_u32 s3, 1
	s_cselect_b64 s[4:5], -1, 0
	s_and_b64 vcc, exec, s[4:5]
	s_cbranch_vccz .LBB0_155
	s_lshl_b32 s3, s85, 3
	s_add_i32 s3, s3, s67
	v_and_b32_e32 v194, 15, v0
	s_cmp_gt_i32 s3, 0x9bff
	v_lshlrev_b32_e32 v195, 2, v0
	s_cbranch_scc1 .LBB0_191
	s_cmp_gt_i32 s3, 0x81ff
	s_cbranch_scc0 .LBB0_156
	s_add_i32 s5, s3, 0xffff7e00
	s_lshr_b32 s4, s5, 8
	s_lshr_b32 s6, s3, 5
	v_readlane_b32 s7, v253, 4
	s_and_b32 s6, s6, 6
	s_bfe_u32 s30, s7, 0x10006
	s_lshl_b32 s8, s4, 20
	s_mov_b32 s9, 0
	s_or_b32 s10, s6, s30
	s_lshl_b64 s[6:7], s[8:9], 2
	s_add_u32 s6, s54, s6
	s_addc_u32 s7, s55, s7
	s_cmpk_lt_u32 s5, 0x4000
	s_cselect_b32 s5, s7, s59
	s_cselect_b32 s6, s6, s58
	s_lshl_b32 s8, s10, 6
	s_lshl_b32 s7, s10, 19
	s_add_u32 s6, s6, s7
	s_addc_u32 s5, s5, 0
	s_lshl_b32 s7, s3, 5
	s_and_b32 s10, s7, 0x7c0
	s_lshl_b32 s7, s10, 2
	s_add_u32 s6, s6, s7
	s_addc_u32 s7, s5, 0
	s_mov_b32 s5, s9
	s_lshl_b64 s[4:5], s[4:5], 20
	s_add_u32 s4, s96, s4
	s_addc_u32 s5, s97, s5
	s_lshl_b32 s9, s10, 9
	s_add_u32 s4, s4, s9
	s_addc_u32 s5, s5, 0
	s_add_u32 s4, s4, s8
	s_addc_u32 s5, s5, 0
	s_add_u32 s18, s4, 0x13000000
	s_addc_u32 s19, s5, 0
	s_cbranch_execz .LBB0_157
	s_mov_b32 s24, 4.0
	s_movk_i32 s31, 0x200
	s_mov_b64 s[4:5], 0x800
	s_branch .LBB0_158

; __device__ __forceinline__ unsigned pk2c(float lo, float hi) { const bf16x2_t r = __builtin_convertvector((f32x2){lo, hi}, bf16x2_t); return __builtin_bit_cast(unsigned, r); }
; __device__ __forceinline__ CvItem cv_decode(const void* const* in, unsigned char* ws, int r) {
;     constexpr int I_EI = 32 * 16, I_EO = 8 * 32; CvItem c;
;     if (r < 65 * I_EI) { const int e = r / I_EI, q = r % I_EI, kb = 2 * ((q >> 1) / 16) + (q & 1), nb = (q >> 1) % 16, n0 = 64 * nb, j = n0 & 511, up = n0 >> 9;
;         const float* W = (e < 64) ? (const float*)in[20] + (size_t)e * DM * 1024 : (const float*)in[22];
;         c.src = W + (size_t)(64 * kb) * 1024 + n0; c.N = 1024; c.K = DM; c.scale = SC_WEI;
;         c.dst = ws + WS_WEI + (size_t)e * 1024 * DM + (size_t)((j >> 7) * 256 + up * 128 + (j & 127)) * DM + 64 * kb; }
;     else { r -= 65 * I_EI; const int e = r / I_EO, q = r % I_EO, kb = 2 * ((q >> 1) / 32) + (q & 1), nb = (q >> 1) % 32;
;         const float* W = (e < 64) ? (const float*)in[21] + (size_t)e * EH * DM : (const float*)in[23];
;         c.src = W + (size_t)(64 * kb) * DM + 64 * nb; c.N = DM; c.K = EH; c.scale = SC_WEO;
;         c.dst = ws + WS_WEO + (size_t)e * DM * EH + (size_t)(64 * nb) * EH + 64 * kb; }
;     return c;
; }
; __device__ __forceinline__ void p2_convert_experts(Ctx& F) {
;     const int gw = F.vcu * NWAVES + F.wave, NGW = F.G * NWAVES, lane = F.lane, li = lane & 15, lg = lane >> 4;
;     constexpr int NCV = 65 * (32 * 16 + 8 * 32);
;     int it = gw; CvItem cur; f32x4 v[16];
;     const int krow = 16 * (li >> 2) + (li & 3);
;     ...
;     if (it < NCV) { cur = cv_decode(F.in, F.ws, it); CV_LOAD(cur); }
;     while (it < NCV) {
;         bf16x8 a[2][4];
; #pragma unroll
;         for (int nh = 0; nh < 2; ++nh)
; #pragma unroll
;             for (int q = 0; q < 4; ++q) { const f32x4 lo = v[(nh * 4 + q) * 2], hi = v[(nh * 4 + q) * 2 + 1];
;                 const u32x4 pk = (u32x4){pk2c(lo.x, lo.y), pk2c(lo.z, lo.w), pk2c(hi.x, hi.y), pk2c(hi.z, hi.w)}; a[nh][q] = __builtin_bit_cast(bf16x8, pk); }
;         const CvItem me = cur; const int nit = it + NGW;
;         if (nit < NCV) { cur = cv_decode(F.in, F.ws, nit); CV_LOAD(cur); }
.LBB0_162:
	s_add_i32 s3, s3, s33
	s_cmp_gt_i32 s3, 0x9bff
	s_cselect_b64 s[16:17], -1, 0
	s_and_b64 vcc, exec, s[16:17]
	s_cbranch_vccnz .LBB0_169
	s_cmp_gt_i32 s3, 0x81ff
	s_mov_b64 s[22:23], -1
	s_cbranch_scc0 .LBB0_165
	s_add_i32 s15, s3, 0xffff7e00
	s_lshr_b32 s12, s3, 5
	s_lshr_b32 s14, s15, 8
	s_and_b32 s12, s12, 6
	s_or_b32 s22, s12, s30
	s_lshl_b32 s12, s14, 20
	s_lshl_b64 s[20:21], s[12:13], 2
	s_add_u32 s12, s54, s20
	s_addc_u32 s20, s55, s21
	s_cmpk_lt_u32 s15, 0x4000
	s_cselect_b32 s15, s20, s59
	s_cselect_b32 s23, s12, s58
	s_lshl_b32 s12, s22, 6
	s_lshl_b64 s[20:21], s[12:13], 13
	s_add_u32 s20, s23, s20
	s_addc_u32 s15, s15, s21
	s_and_b32 s22, s42, 0x7c0
	s_lshl_b32 s21, s22, 2
	s_add_u32 s20, s20, s21
	s_addc_u32 s21, s15, 0
	s_mov_b32 s15, s13
	s_lshl_b64 s[14:15], s[14:15], 20
	s_add_u32 s14, s35, s14
	s_addc_u32 s15, s36, s15
	s_lshl_b32 s22, s22, 9
	s_add_u32 s14, s14, s22
	s_addc_u32 s15, s15, 0
	s_add_u32 s14, s14, s12
	s_addc_u32 s15, s15, 0
	s_mov_b64 s[22:23], 0

; #define CV_LOAD(c) do { _Pragma("unroll") for (int nh = 0; nh < 2; ++nh) _Pragma("unroll") for (int q = 0; q < 4; ++q) { const float* p_ = (c).src + (size_t)(krow + 4 * q) * (c).N + 32 * nh + 8 * lg; \
;         v[(nh * 4 + q) * 2] = *(const f32x4*)p_; v[(nh * 4 + q) * 2 + 1] = *(const f32x4*)(p_ + 4); } } while (0)
; __device__ __forceinline__ CvItem cv_decode(const void* const* in, unsigned char* ws, int r) {
;     constexpr int I_EI = 32 * 16, I_EO = 8 * 32; CvItem c;
;     if (r < 65 * I_EI) { const int e = r / I_EI, q = r % I_EI, kb = 2 * ((q >> 1) / 16) + (q & 1), nb = (q >> 1) % 16, n0 = 64 * nb, j = n0 & 511, up = n0 >> 9;
;         const float* W = (e < 64) ? (const float*)in[20] + (size_t)e * DM * 1024 : (const float*)in[22];
;         c.src = W + (size_t)(64 * kb) * 1024 + n0; c.N = 1024; c.K = DM; c.scale = SC_WEI;
;         c.dst = ws + WS_WEI + (size_t)e * 1024 * DM + (size_t)((j >> 7) * 256 + up * 128 + (j & 127)) * DM + 64 * kb; }
;     else { r -= 65 * I_EI; const int e = r / I_EO, q = r % I_EO, kb = 2 * ((q >> 1) / 32) + (q & 1), nb = (q >> 1) % 32;
;         const float* W = (e < 64) ? (const float*)in[21] + (size_t)e * EH * DM : (const float*)in[23];
;         c.src = W + (size_t)(64 * kb) * DM + 64 * nb; c.N = DM; c.K = EH; c.scale = SC_WEO;
;         c.dst = ws + WS_WEO + (size_t)e * DM * EH + (size_t)(64 * nb) * EH + 64 * kb; }
;     return c;
; }
; __device__ __forceinline__ void p2_convert_experts(Ctx& F) {
;     const int gw = F.vcu * NWAVES + F.wave, NGW = F.G * NWAVES, lane = F.lane, li = lane & 15, lg = lane >> 4;
;     constexpr int NCV = 65 * (32 * 16 + 8 * 32);
;     int it = gw; CvItem cur; f32x4 v[16];
;     const int krow = 16 * (li >> 2) + (li & 3);
;     ...
;     if (it < NCV) { cur = cv_decode(F.in, F.ws, it); CV_LOAD(cur); }
;     while (it < NCV) {
; __global__ void __launch_bounds__(NWAVES * 64, 2) fwd_kernel(Args args) {
;     ...
;         if (!(F.vcu & 1)) p2_convert_experts(F);
.LBB0_214:
	s_andn2_b64 vcc, exec, s[0:1]
	s_cbranch_vccnz .LBB0_254
	s_lshl_b32 s0, s85, 3
	s_add_i32 s3, s0, s67
	s_cmp_gt_i32 s3, 0x9bff
	s_cbranch_scc1 .LBB0_254
	s_cmp_gt_i32 s3, 0x81ff
	s_cbranch_scc0 .LBB0_219
	s_add_i32 s1, s3, 0xffff7e00
	s_lshr_b32 s0, s1, 8
	s_lshr_b32 s4, s3, 5
	v_readlane_b32 s5, v253, 4
	s_and_b32 s4, s4, 6
	s_bfe_u32 s28, s5, 0x10006
	s_lshl_b32 s6, s0, 20
	s_mov_b32 s7, 0
	s_or_b32 s8, s4, s28
	s_lshl_b64 s[4:5], s[6:7], 2
	s_add_u32 s4, s54, s4
	s_addc_u32 s5, s55, s5
	s_cmpk_lt_u32 s1, 0x4000
	s_cselect_b32 s1, s5, s59
	s_cselect_b32 s4, s4, s58
	s_lshl_b32 s6, s8, 6
	s_lshl_b32 s5, s8, 19
	s_add_u32 s4, s4, s5
	s_addc_u32 s1, s1, 0
	s_lshl_b32 s5, s3, 5
	s_and_b32 s8, s5, 0x7c0
	s_lshl_b32 s5, s8, 2
	s_add_u32 s4, s4, s5
	s_addc_u32 s5, s1, 0
	s_mov_b32 s1, s7
	s_lshl_b64 s[0:1], s[0:1], 20
	s_add_u32 s0, s96, s0
	s_addc_u32 s1, s97, s1
	s_lshl_b32 s7, s8, 9
	s_add_u32 s0, s0, s7
	s_addc_u32 s1, s1, 0
	s_add_u32 s0, s0, s6
	s_addc_u32 s1, s1, 0
	s_add_u32 s16, s0, 0x13000000
	s_addc_u32 s17, s1, 0
	s_cbranch_execz .LBB0_220
	s_mov_b32 s22, 4.0
	s_movk_i32 s29, 0x200
	s_mov_b64 s[0:1], 0x800
	s_branch .LBB0_221

; __device__ __forceinline__ unsigned pk2c(float lo, float hi) { const bf16x2_t r = __builtin_convertvector((f32x2){lo, hi}, bf16x2_t); return __builtin_bit_cast(unsigned, r); }
; __device__ __forceinline__ CvItem cv_decode(const void* const* in, unsigned char* ws, int r) {
;     constexpr int I_EI = 32 * 16, I_EO = 8 * 32; CvItem c;
;     if (r < 65 * I_EI) { const int e = r / I_EI, q = r % I_EI, kb = 2 * ((q >> 1) / 16) + (q & 1), nb = (q >> 1) % 16, n0 = 64 * nb, j = n0 & 511, up = n0 >> 9;
;         const float* W = (e < 64) ? (const float*)in[20] + (size_t)e * DM * 1024 : (const float*)in[22];
;         c.src = W + (size_t)(64 * kb) * 1024 + n0; c.N = 1024; c.K = DM; c.scale = SC_WEI;
;         c.dst = ws + WS_WEI + (size_t)e * 1024 * DM + (size_t)((j >> 7) * 256 + up * 128 + (j & 127)) * DM + 64 * kb; }
;     else { r -= 65 * I_EI; const int e = r / I_EO, q = r % I_EO, kb = 2 * ((q >> 1) / 32) + (q & 1), nb = (q >> 1) % 32;
;         const float* W = (e < 64) ? (const float*)in[21] + (size_t)e * EH * DM : (const float*)in[23];
;         c.src = W + (size_t)(64 * kb) * DM + 64 * nb; c.N = DM; c.K = EH; c.scale = SC_WEO;
;         c.dst = ws + WS_WEO + (size_t)e * DM * EH + (size_t)(64 * nb) * EH + 64 * kb; }
;     return c;
; }
; __device__ __forceinline__ void p2_convert_experts(Ctx& F) {
;     const int gw = F.vcu * NWAVES + F.wave, NGW = F.G * NWAVES, lane = F.lane, li = lane & 15, lg = lane >> 4;
;     constexpr int NCV = 65 * (32 * 16 + 8 * 32);
;     int it = gw; CvItem cur; f32x4 v[16];
;     const int krow = 16 * (li >> 2) + (li & 3);
;     ...
;     if (it < NCV) { cur = cv_decode(F.in, F.ws, it); CV_LOAD(cur); }
;     while (it < NCV) {
;         bf16x8 a[2][4];
; #pragma unroll
;         for (int nh = 0; nh < 2; ++nh)
; #pragma unroll
;             for (int q = 0; q < 4; ++q) { const f32x4 lo = v[(nh * 4 + q) * 2], hi = v[(nh * 4 + q) * 2 + 1];
;                 const u32x4 pk = (u32x4){pk2c(lo.x, lo.y), pk2c(lo.z, lo.w), pk2c(hi.x, hi.y), pk2c(hi.z, hi.w)}; a[nh][q] = __builtin_bit_cast(bf16x8, pk); }
;         const CvItem me = cur; const int nit = it + NGW;
;         if (nit < NCV) { cur = cv_decode(F.in, F.ws, nit); CV_LOAD(cur); }
.LBB0_225:
	s_add_i32 s3, s3, s30
	s_cmp_gt_i32 s3, 0x9bff
	s_cselect_b64 s[14:15], -1, 0
	s_and_b64 vcc, exec, s[14:15]
	s_cbranch_vccnz .LBB0_232
	s_cmp_gt_i32 s3, 0x81ff
	s_mov_b64 s[20:21], -1
	s_cbranch_scc0 .LBB0_228
	s_add_i32 s13, s3, 0xffff7e00
	s_lshr_b32 s0, s3, 5
	s_lshr_b32 s12, s13, 8
	s_and_b32 s0, s0, 6
	s_or_b32 s20, s0, s28
	s_lshl_b32 s0, s12, 20
	s_lshl_b64 s[18:19], s[0:1], 2
	s_add_u32 s0, s54, s18
	s_addc_u32 s18, s55, s19
	s_cmpk_lt_u32 s13, 0x4000
	s_cselect_b32 s13, s18, s59
	s_cselect_b32 s21, s0, s58
	s_lshl_b32 s0, s20, 6
	s_lshl_b64 s[18:19], s[0:1], 13
	s_add_u32 s18, s21, s18
	s_addc_u32 s13, s13, s19
	s_and_b32 s20, s40, 0x7c0
	s_lshl_b32 s19, s20, 2
	s_add_u32 s18, s18, s19
	s_addc_u32 s19, s13, 0
	s_mov_b32 s13, s1
	s_lshl_b64 s[12:13], s[12:13], 20
	s_add_u32 s12, s33, s12
	s_addc_u32 s13, s34, s13
	s_lshl_b32 s20, s20, 9
	s_add_u32 s12, s12, s20
	s_addc_u32 s13, s13, 0
	s_add_u32 s12, s12, s0
	s_addc_u32 s13, s13, 0
	s_mov_b64 s[20:21], 0

; #define CV_LOAD(c) do { _Pragma("unroll") for (int nh = 0; nh < 2; ++nh) _Pragma("unroll") for (int q = 0; q < 4; ++q) { const float* p_ = (c).src + (size_t)(krow + 4 * q) * (c).N + 32 * nh + 8 * lg; \
;         v[(nh * 4 + q) * 2] = *(const f32x4*)p_; v[(nh * 4 + q) * 2 + 1] = *(const f32x4*)(p_ + 4); } } while (0)
; __device__ __forceinline__ CvItem cv_decode(const void* const* in, unsigned char* ws, int r) {
;     constexpr int I_EI = 32 * 16, I_EO = 8 * 32; CvItem c;
;     if (r < 65 * I_EI) { const int e = r / I_EI, q = r % I_EI, kb = 2 * ((q >> 1) / 16) + (q & 1), nb = (q >> 1) % 16, n0 = 64 * nb, j = n0 & 511, up = n0 >> 9;
;         const float* W = (e < 64) ? (const float*)in[20] + (size_t)e * DM * 1024 : (const float*)in[22];
;         c.src = W + (size_t)(64 * kb) * 1024 + n0; c.N = 1024; c.K = DM; c.scale = SC_WEI;
;         c.dst = ws + WS_WEI + (size_t)e * 1024 * DM + (size_t)((j >> 7) * 256 + up * 128 + (j & 127)) * DM + 64 * kb; }
;     else { r -= 65 * I_EI; const int e = r / I_EO, q = r % I_EO, kb = 2 * ((q >> 1) / 32) + (q & 1), nb = (q >> 1) % 32;
;         const float* W = (e < 64) ? (const float*)in[21] + (size_t)e * EH * DM : (const float*)in[23];
;         c.src = W + (size_t)(64 * kb) * DM + 64 * nb; c.N = DM; c.K = EH; c.scale = SC_WEO;
;         c.dst = ws + WS_WEO + (size_t)e * DM * EH + (size_t)(64 * nb) * EH + 64 * kb; }
;     return c;
; __device__ __forceinline__ void p2_convert_experts(Ctx& F) {
;     const int gw = F.vcu * NWAVES + F.wave, NGW = F.G * NWAVES, lane = F.lane, li = lane & 15, lg = lane >> 4;
;     constexpr int NCV = 65 * (32 * 16 + 8 * 32);
;     int it = gw; CvItem cur; f32x4 v[16];
;     const int krow = 16 * (li >> 2) + (li & 3);
;     ...
;     if (it < NCV) { cur = cv_decode(F.in, F.ws, it); CV_LOAD(cur); }
.Lc3_entry:
	v_readlane_b32 s67, v253, 57
	v_readlane_b32 s84, v253, 58
	v_readlane_b32 s85, v253, 59
	v_readlane_b32 s52, v253, 49
	v_readlane_b32 s53, v253, 50
	v_readlane_b32 s54, v253, 51
	v_readlane_b32 s55, v253, 52
	v_readlane_b32 s56, v253, 53
	v_readlane_b32 s57, v253, 54
	v_readlane_b32 s58, v253, 55
	v_readlane_b32 s59, v253, 56
	v_and_b32_e32 v194, 15, v0
	v_lshlrev_b32_e32 v195, 2, v0
	v_lshrrev_b32_e32 v2, 1, v0
	v_lshlrev_b32_e32 v197, 4, v0
	v_and_b32_e32 v196, 24, v2
	s_nop 3
	s_lshr_b32 s0, s85, 1
	s_lshl_b32 s0, s0, 3
	s_add_i32 s3, s0, s67
	s_add_i32 s3, s3, 0x9c00
	s_cmp_gt_i32 s3, 0xc2ff
	s_cbranch_scc1 .Lc3_end
	s_cmp_gt_i32 s3, 0x81ff
	s_cbranch_scc0 .Lc3_219
	s_add_i32 s1, s3, 0xffff7e00
	s_lshr_b32 s0, s1, 8
	s_lshr_b32 s4, s3, 5
	v_readlane_b32 s5, v253, 4
	s_and_b32 s4, s4, 6
	s_bfe_u32 s28, s5, 0x10006
	s_lshl_b32 s6, s0, 20
	s_mov_b32 s7, 0
	s_or_b32 s8, s4, s28
	s_lshl_b64 s[4:5], s[6:7], 2
	s_add_u32 s4, s54, s4
	s_addc_u32 s5, s55, s5
	s_cmpk_lt_u32 s1, 0x4000
	s_cselect_b32 s1, s5, s59
	s_cselect_b32 s4, s4, s58
	s_lshl_b32 s6, s8, 6
	s_lshl_b32 s5, s8, 19
	s_add_u32 s4, s4, s5
	s_addc_u32 s1, s1, 0
	s_lshl_b32 s5, s3, 5
	s_and_b32 s8, s5, 0x7c0
	s_lshl_b32 s5, s8, 2
	s_add_u32 s4, s4, s5
	s_addc_u32 s5, s1, 0
	s_mov_b32 s1, s7
	s_lshl_b64 s[0:1], s[0:1], 20
	s_add_u32 s0, s96, s0
	s_addc_u32 s1, s97, s1
	s_lshl_b32 s7, s8, 9
	s_add_u32 s0, s0, s7
	s_addc_u32 s1, s1, 0
	s_add_u32 s0, s0, s6
	s_addc_u32 s1, s1, 0
	s_add_u32 s16, s0, 0x13000000
	s_addc_u32 s17, s1, 0
	s_cbranch_execz .Lc3_220
	s_mov_b32 s22, 4.0
	s_movk_i32 s29, 0x200
	s_mov_b64 s[0:1], 0x800
	s_branch .Lc3_221

; __device__ __forceinline__ unsigned pk2c(float lo, float hi) { const bf16x2_t r = __builtin_convertvector((f32x2){lo, hi}, bf16x2_t); return __builtin_bit_cast(unsigned, r); }
; #define CV_LOAD(c) do { _Pragma("unroll") for (int nh = 0; nh < 2; ++nh) _Pragma("unroll") for (int q = 0; q < 4; ++q) { const float* p_ = (c).src + (size_t)(krow + 4 * q) * (c).N + 32 * nh + 8 * lg; \
;         v[(nh * 4 + q) * 2] = *(const f32x4*)p_; v[(nh * 4 + q) * 2 + 1] = *(const f32x4*)(p_ + 4); } } while (0)
; __device__ __forceinline__ void p2_convert_experts(Ctx& F) {
;     const int gw = F.vcu * NWAVES + F.wave, NGW = F.G * NWAVES, lane = F.lane, li = lane & 15, lg = lane >> 4;
;     constexpr int NCV = 65 * (32 * 16 + 8 * 32);
;     int it = gw; CvItem cur; f32x4 v[16];
;     const int krow = 16 * (li >> 2) + (li & 3);
;     ...
;     if (it < NCV) { cur = cv_decode(F.in, F.ws, it); CV_LOAD(cur); }
;     while (it < NCV) {
;         bf16x8 a[2][4];
; #pragma unroll
;         for (int nh = 0; nh < 2; ++nh)
; #pragma unroll
;             for (int q = 0; q < 4; ++q) { const f32x4 lo = v[(nh * 4 + q) * 2], hi = v[(nh * 4 + q) * 2 + 1];
;                 const u32x4 pk = (u32x4){pk2c(lo.x, lo.y), pk2c(lo.z, lo.w), pk2c(hi.x, hi.y), pk2c(hi.z, hi.w)}; a[nh][q] = __builtin_bit_cast(bf16x8, pk); }
;         const CvItem me = cur; const int nit = it + NGW;
;         if (nit < NCV) { cur = cv_decode(F.in, F.ws, nit); CV_LOAD(cur); }
;         const unsigned sbits = (unsigned)f2bf(me.scale);
; #pragma unroll
;         for (int h = 0; h < 2; ++h) {
;             u32x4 sel = (u32x4){0u, 0u, 0u, 0u}; { const int d = 16 * h + li - 8 * lg; if (d >= 0 && d < 8) { const unsigned wv = (d & 1) ? (sbits << 16) : sbits; if ((d >> 1) == 0) sel.x = wv; else if ((d >> 1) == 1) sel.y = wv; else if ((d >> 1) == 2) sel.z = wv; else sel.w = wv; } }
.Lc3_221:
	v_and_b32_e32 v2, 3, v0
	v_and_or_b32 v139, v195, 48, v2
	v_or_b32_e32 v141, 12, v139
	v_mov_b32_e32 v135, 0
	v_lshlrev_b32_e32 v134, 2, v196
	v_mul_u32_u24_e32 v2, s0, v141
	v_or_b32_e32 v143, 8, v139
	v_lshl_add_u64 v[10:11], s[4:5], 0, v[134:135]
	v_lshlrev_b32_e32 v134, 2, v2
	v_mul_u32_u24_e32 v14, s0, v143
	v_or_b32_e32 v146, 4, v139
	v_lshl_add_u64 v[12:13], v[10:11], 0, v[134:135]
	v_lshlrev_b32_e32 v134, 2, v14
	v_mul_u32_u24_e32 v16, s0, v146
	v_lshl_add_u64 v[14:15], v[10:11], 0, v[134:135]
	v_lshlrev_b32_e32 v134, 2, v16
	global_load_dwordx4 v[2:5], v[12:13], off offset:144
	global_load_dwordx4 v[6:9], v[12:13], off offset:128
	global_load_dwordx4 v[18:21], v[14:15], off offset:144
	global_load_dwordx4 v[22:25], v[14:15], off offset:128
	v_lshl_add_u64 v[16:17], v[10:11], 0, v[134:135]
	global_load_dwordx4 v[70:73], v[12:13], off
	global_load_dwordx4 v[54:57], v[16:17], off offset:144
	global_load_dwordx4 v[62:65], v[16:17], off offset:128
	global_load_dwordx4 v[94:97], v[14:15], off offset:16
	global_load_dwordx4 v[98:101], v[14:15], off
	v_mul_u32_u24_e32 v14, s0, v139
	v_lshlrev_b32_e32 v134, 2, v14
	v_lshl_add_u64 v[10:11], v[10:11], 0, v[134:135]
	global_load_dwordx4 v[114:117], v[16:17], off offset:16
	global_load_dwordx4 v[118:121], v[16:17], off
	global_load_dwordx4 v[102:105], v[10:11], off offset:144
	global_load_dwordx4 v[106:109], v[10:11], off offset:128
	global_load_dwordx4 v[126:129], v[10:11], off
	global_load_dwordx4 v[122:125], v[10:11], off offset:16
	global_load_dwordx4 v[110:113], v[12:13], off offset:16
	s_lshl_b32 s30, s84, 2
	s_add_u32 s33, s96, 0x13000000
	v_sub_u32_e32 v10, v194, v196
	v_or_b32_e32 v140, 16, v194
	s_addc_u32 s34, s97, 0
	v_cmp_gt_u32_e64 s[4:5], 8, v10
	v_cmp_lt_u32_e64 s[6:7], 1, v10
	v_lshrrev_b32_e32 v149, 1, v10
	v_sub_u32_e32 v10, v140, v196
	s_add_u32 s35, s96, 0x2c00000
	v_cmp_gt_u32_e64 s[8:9], 8, v10
	v_cmp_lt_u32_e64 s[10:11], 1, v10
	v_lshrrev_b32_e32 v150, 1, v10
	s_addc_u32 s36, s97, 0
	s_add_i32 s14, s30, s3
	v_and_b32_e32 v136, 48, v0
	v_and_b32_e32 v147, 16, v197
	v_or_b32_e32 v138, 32, v194
	v_or_b32_e32 v142, 48, v194
	s_mov_b32 s1, 0
	s_mov_b32 s31, 0xc3e00000
	v_mov_b32_e32 v148, 0x43e00000
	s_mov_b32 s0, s22
	s_mov_b32 s41, s29
	s_mov_b64 s[12:13], s[16:17]
	v_mov_b32_e32 v137, v135
	s_lshl_b32 s37, s84, 8
	s_lshl_b32 s38, s84, 7
	s_lshl_b32 s39, s14, 6
	s_lshl_b32 s40, s14, 5
	v_lshlrev_b32_e32 v134, 2, v196
	s_waitcnt vmcnt(0)
	v_mov_b64_e32 v[42:43], v[70:71]
	v_mov_b64_e32 v[80:81], v[4:5]
	v_mov_b64_e32 v[84:85], v[8:9]
	v_mov_b64_e32 v[88:89], v[20:21]
	v_mov_b64_e32 v[92:93], v[24:25]
	v_mov_b64_e32 v[34:35], v[98:99]
	v_mov_b64_e32 v[38:39], v[94:95]
	v_mov_b64_e32 v[68:69], v[56:57]
	v_mov_b64_e32 v[76:77], v[64:65]
	v_mov_b64_e32 v[26:27], v[118:119]
	v_mov_b64_e32 v[30:31], v[114:115]
	v_mov_b64_e32 v[50:51], v[102:103]
	v_mov_b64_e32 v[58:59], v[106:107]
	v_mov_b64_e32 v[10:11], v[126:127]
	v_mov_b64_e32 v[14:15], v[122:123]
	v_mov_b64_e32 v[46:47], v[110:111]
	v_mov_b64_e32 v[78:79], v[2:3]
	v_mov_b64_e32 v[82:83], v[6:7]
	v_mov_b64_e32 v[44:45], v[72:73]
	v_mov_b64_e32 v[86:87], v[18:19]
	v_mov_b64_e32 v[90:91], v[22:23]
	v_mov_b64_e32 v[36:37], v[100:101]
	v_mov_b64_e32 v[40:41], v[96:97]
	v_mov_b64_e32 v[66:67], v[54:55]
	v_mov_b64_e32 v[74:75], v[62:63]
	v_mov_b64_e32 v[28:29], v[120:121]
	v_mov_b64_e32 v[32:33], v[116:117]
	v_mov_b64_e32 v[52:53], v[104:105]
	v_mov_b64_e32 v[60:61], v[108:109]
	v_mov_b64_e32 v[12:13], v[128:129]
	v_mov_b64_e32 v[16:17], v[124:125]
	v_mov_b64_e32 v[48:49], v[112:113]
	s_branch .Lc3_225

; __device__ __forceinline__ unsigned xb_add(unsigned* p, unsigned v) { return __hip_atomic_fetch_add(p, v, __ATOMIC_RELAXED, __HIP_MEMORY_SCOPE_AGENT); }
; #define GRID_BAR() xcd_barrier(bar)
; #define GRID_BAR() do { } while (0)
; #define BOTH(k) (IN(k) && IN((k) + 1))
; __device__ __forceinline__ void xcd_barrier(const XcdBarrier& b) {
;     asm volatile("s_waitcnt vmcnt(0)" ::: "memory");
;     __syncthreads();
;     if (threadIdx.x == 0) {
;         unsigned* bar = b.bar;
;         __builtin_amdgcn_s_waitcnt(0);
;         unsigned nloc = b.st[0], nx = b.st[1];
;         if (nloc == 0u) { xcd_barrier_complete(bar, b.x, nloc, nx); b.st[0] = nloc; b.st[1] = nx; }
;         const unsigned old = xb_add(&bar[XB_XSUB(b.x)], 1u);
; __global__ void __launch_bounds__(NWAVES * 64, 2) fwd_kernel(Args args) {
;     ...
;         if (BOTH(3)) GRID_BAR();
.Lc3_end:
.LBB0_383:
	v_readlane_b32 s86, v253, 60
	v_readlane_b32 s87, v253, 61
	s_cmp_lt_i32 s87, 5
	v_readlane_b32 s84, v253, 58
	v_readlane_b32 s85, v253, 59
	s_cbranch_scc1 .LBB0_437
	s_waitcnt vmcnt(0)
	s_waitcnt vmcnt(0)
	s_barrier
	s_and_saveexec_b64 s[0:1], s[92:93]
	s_cbranch_execz .LBB0_436
	s_add_i32 s3, 0, 0x27f00
	v_mov_b32_e32 v2, s3
	s_waitcnt vmcnt(0) expcnt(0) lgkmcnt(0)
	ds_read_b32 v4, v2
	s_add_i32 s3, 0, 0x27f04
	v_mov_b32_e32 v2, s3
	ds_read_b32 v2, v2
	s_waitcnt lgkmcnt(1)
	v_cmp_ne_u32_e32 vcc, 0, v4
	s_cbranch_vccnz .LBB0_400
	v_readlane_b32 s4, v253, 5
	v_readlane_b32 s5, v253, 6
	s_load_dwordx2 s[8:9], s[4:5], 0x4
	s_add_u32 s4, s96, 0x4200
	s_addc_u32 s5, s97, 0
	s_add_u32 s6, s96, 0x4400
	s_addc_u32 s7, s97, 0
	s_waitcnt lgkmcnt(0)
	s_mul_i32 s3, s8, s84
	s_add_u32 s8, s96, 0x4500
	s_mul_i32 s3, s3, s9
	s_addc_u32 s9, s97, 0
	s_add_u32 s10, s96, 0x4600
	s_addc_u32 s11, s97, 0
	s_add_u32 s12, s96, 0x4700
	s_addc_u32 s13, s97, 0
	s_add_u32 s14, s96, 0x4800
	s_addc_u32 s15, s97, 0
	s_add_u32 s16, s96, 0x4900
	s_addc_u32 s17, s97, 0
	s_add_u32 s18, s96, 0x4a00
	s_addc_u32 s19, s97, 0
	s_add_u32 s20, s96, 0x4b00
	s_addc_u32 s21, s97, 0
	s_add_u32 s22, s96, 0x4c00
	s_addc_u32 s23, s97, 0
	s_add_u32 s24, s96, 0x4d00
	s_addc_u32 s25, s97, 0
	s_add_u32 s26, s96, 0x4e00
	s_addc_u32 s27, s97, 0
	s_add_u32 s28, s96, 0x4f00
	s_addc_u32 s29, s97, 0
	s_add_u32 s30, s96, 0x5000
	s_addc_u32 s31, s97, 0
	s_add_u32 s34, s96, 0x5100
	s_addc_u32 s35, s97, 0
	s_add_u32 s36, s96, 0x5200
	s_addc_u32 s37, s97, 0
	s_add_u32 s38, s96, 0x5300
	s_addc_u32 s39, s97, 0
	s_mov_b32 s33, 1
	v_mov_b32_e32 v18, 0
	s_branch .LBB0_388

; #define G8_BAR __builtin_amdgcn_s_barrier()
; template <class Epi, class Sched, int NT, bool F8 = false>
; __device__ __forceinline__ void gemm_phase(LAS unsigned char* lds, const Sched& S, const Epi& E) {
;     ...
;         if (!has_next) break;
; #pragma unroll
;         for (int a = 0; a < 2; ++a)
; #pragma unroll
;             for (int b = 0; b < 2; ++b)
; #pragma unroll
;                 for (int m = 0; m < 4; ++m)
; #pragma unroll
;                     for (int n = 0; n < 2; ++n) acc[a][b][m][n] = (f32x4){0.f, 0.f, 0.f, 0.f};
;         cur = nxt; cA = nA; cB = nB; ++ui;
;         if (wr == 1) G8_BAR;
.LBB0_841:
	s_add_u32 s26, s26, 0x80
	s_addc_u32 s27, s27, 0
	s_add_u32 s19, s28, 0x100
	v_mov_b32_e32 v66, 0
	v_mov_b32_e32 v205, v195
	v_mov_b32_e32 v207, v195
	s_addc_u32 s57, s29, 0
	s_mov_b32 s58, -2
	s_branch .LBB0_844

; #define G8_STAGE(bufoff, gbase, voff) do { _Pragma("unroll") for (int _i = 0; _i < 2; ++_i) \
;         __builtin_amdgcn_global_load_lds((const unsigned*)((const char*)(gbase) + (voff)[_i]), (LAS unsigned*)(lds + (bufoff) + ldsw + _i * 8192), 16, 0, 0); } while (0)
; #define G8_LDA(dst, b, h) do { _Pragma("unroll") for (int m = 0; m < 4; ++m) _Pragma("unroll") for (int k = 0; k < 2; ++k) dst[m][k] = *(const LAS bf16x8*)(lds + G8_SA(b, h) + aoff + m * 2048 + k * 1024); } while (0)
; #define G8_WAIT_L(n) asm volatile("s_waitcnt lgkmcnt(" #n ")" ::: "memory")
; #define G8_BAR __builtin_amdgcn_s_barrier()
; #define G8_SCHED __builtin_amdgcn_sched_barrier(0)
; template <class Epi, class Sched, int NT, bool F8 = false>
; __device__ __forceinline__ void gemm_phase(LAS unsigned char* lds, const Sched& S, const Epi& E) {
;     ...
;             G8_WAIT_VF(t, ui); G8_WAIT_L(0); G8_BAR; G8_MMA(0, 0, At, B0); G8_MMA(0, 1, At, B1); G8_BAR; G8_SCHED;
;             G8_LDA(At, 0, 1); G8_STAGE(G8_SB(0, 0), b2, voffB); G8_STAGE(G8_SB(0, 1), b2, voffB1); G8_STAGE(G8_SA(0, 0), a2, cur.vA0);
.Lg8e4:
	s_waitcnt lgkmcnt(0)
	s_barrier
	s_setprio 1
	s_waitcnt lgkmcnt(0)
	s_cmp_eq_u32 s58, 0
	s_cbranch_scc1 .Lcz_p80
	v_mfma_scale_f32_16x16x128_f8f6f4 v[190:193], v[18:25], v[58:65], v[190:193], v227, v227 op_sel_hi:[0,0,0]
	v_mfma_scale_f32_16x16x128_f8f6f4 v[182:185], v[26:33], v[58:65], v[182:185], v227, v227 op_sel_hi:[0,0,0]
	v_mfma_scale_f32_16x16x128_f8f6f4 v[174:177], v[18:25], v[50:57], v[174:177], v227, v227 op_sel_hi:[0,0,0]
	v_mfma_scale_f32_16x16x128_f8f6f4 v[166:169], v[26:33], v[50:57], v[166:169], v227, v227 op_sel_hi:[0,0,0]
	v_mfma_scale_f32_16x16x128_f8f6f4 v[158:161], v[18:25], v[42:49], v[158:161], v227, v227 op_sel_hi:[0,0,0]
	v_mfma_scale_f32_16x16x128_f8f6f4 v[150:153], v[26:33], v[42:49], v[150:153], v227, v227 op_sel_hi:[0,0,0]
	v_mfma_scale_f32_16x16x128_f8f6f4 v[142:145], v[18:25], v[34:41], v[142:145], v227, v227 op_sel_hi:[0,0,0]
	v_mfma_scale_f32_16x16x128_f8f6f4 v[134:137], v[26:33], v[34:41], v[134:137], v227, v227 op_sel_hi:[0,0,0]
	s_setprio 0
	s_setprio 1
	v_mfma_scale_f32_16x16x128_f8f6f4 v[186:189], v[2:9], v[58:65], v[186:189], v227, v227 op_sel_hi:[0,0,0]
	v_mfma_scale_f32_16x16x128_f8f6f4 v[178:181], v[10:17], v[58:65], v[178:181], v227, v227 op_sel_hi:[0,0,0]
	v_mfma_scale_f32_16x16x128_f8f6f4 v[170:173], v[2:9], v[50:57], v[170:173], v227, v227 op_sel_hi:[0,0,0]
	v_mfma_scale_f32_16x16x128_f8f6f4 v[162:165], v[10:17], v[50:57], v[162:165], v227, v227 op_sel_hi:[0,0,0]
	v_mfma_scale_f32_16x16x128_f8f6f4 v[154:157], v[2:9], v[42:49], v[154:157], v227, v227 op_sel_hi:[0,0,0]
	v_mfma_scale_f32_16x16x128_f8f6f4 v[146:149], v[10:17], v[42:49], v[146:149], v227, v227 op_sel_hi:[0,0,0]
	v_mfma_scale_f32_16x16x128_f8f6f4 v[138:141], v[2:9], v[34:41], v[138:141], v227, v227 op_sel_hi:[0,0,0]
	v_mfma_scale_f32_16x16x128_f8f6f4 v[130:133], v[10:17], v[34:41], v[130:133], v227, v227 op_sel_hi:[0,0,0]
.Lcz_p80r:
	s_setprio 0
	s_barrier
	s_mov_b32 m0, s40
	v_lshl_add_u64 v[232:233], s[34:35], 0, v[196:197]
	ds_read_b128 v[34:37], v226 offset:16384
	ds_read_b128 v[38:41], v226 offset:17408
	ds_read_b128 v[42:45], v226 offset:18432
	ds_read_b128 v[46:49], v226 offset:19456
	ds_read_b128 v[50:53], v226 offset:20480
	ds_read_b128 v[54:57], v226 offset:21504
	ds_read_b128 v[58:61], v226 offset:22528
	ds_read_b128 v[62:65], v226 offset:23552
	global_load_lds_dwordx4 v[232:233], off
	v_lshl_add_u64 v[234:235], s[34:35], 0, v[200:201]
	s_mov_b32 m0, s41
	v_lshl_add_u64 v[236:237], s[34:35], 0, v[198:199]
	global_load_lds_dwordx4 v[234:235], off
	s_mov_b32 m0, s42
	v_mov_b32_e32 v213, v195
	global_load_lds_dwordx4 v[236:237], off
	v_lshl_add_u64 v[236:237], s[34:35], 0, v[202:203]
	s_mov_b32 m0, s43
	v_lshl_add_u64 v[238:239], s[30:31], 0, v[212:213]
	global_load_lds_dwordx4 v[236:237], off
	s_mov_b32 m0, s33
	v_lshl_add_u64 v[236:237], s[30:31], 0, v[194:195]
	global_load_lds_dwordx4 v194, s[30:31]
	s_mov_b32 m0, s44
	s_nop 0
	global_load_lds_dwordx4 v212, s[30:31]
	s_cmp_lg_u32 s58, 0
	s_cbranch_scc1 .Lg8s5
	s_cmp_eq_u32 s56, 0
	s_cbranch_scc1 .Lg8s5
	s_waitcnt vmcnt(12)
	s_branch .Lg8e5

; #define G8_WAIT_L(n) asm volatile("s_waitcnt lgkmcnt(" #n ")" ::: "memory")
; #define G8_BAR __builtin_amdgcn_s_barrier()
; #define G8_SCHED __builtin_amdgcn_sched_barrier(0)
; template <class Epi, class Sched, int NT, bool F8 = false>
; __device__ __forceinline__ void gemm_phase(LAS unsigned char* lds, const Sched& S, const Epi& E) {
;     ...
;             G8_WAIT_VF(t, ui); G8_WAIT_L(0); G8_BAR; G8_MMA(1, 0, At, B0); G8_MMA(1, 1, At, B1); G8_BAR; G8_SCHED;
.Lg8e5:
	s_waitcnt lgkmcnt(0)
	s_barrier
	s_setprio 1
	s_waitcnt lgkmcnt(0)
	s_cmp_eq_u32 s58, 0
	s_cbranch_scc1 .Lcz_p81
	v_mfma_scale_f32_16x16x128_f8f6f4 v[126:129], v[18:25], v[34:41], v[126:129], v227, v227 op_sel_hi:[0,0,0]
	v_mfma_scale_f32_16x16x128_f8f6f4 v[118:121], v[26:33], v[34:41], v[118:121], v227, v227 op_sel_hi:[0,0,0]
	v_mfma_scale_f32_16x16x128_f8f6f4 v[110:113], v[18:25], v[42:49], v[110:113], v227, v227 op_sel_hi:[0,0,0]
	v_mfma_scale_f32_16x16x128_f8f6f4 v[102:105], v[26:33], v[42:49], v[102:105], v227, v227 op_sel_hi:[0,0,0]
	v_mfma_scale_f32_16x16x128_f8f6f4 v[94:97], v[18:25], v[50:57], v[94:97], v227, v227 op_sel_hi:[0,0,0]
	v_mfma_scale_f32_16x16x128_f8f6f4 v[86:89], v[26:33], v[50:57], v[86:89], v227, v227 op_sel_hi:[0,0,0]
	v_mfma_scale_f32_16x16x128_f8f6f4 v[78:81], v[18:25], v[58:65], v[78:81], v227, v227 op_sel_hi:[0,0,0]
	v_mfma_scale_f32_16x16x128_f8f6f4 v[70:73], v[26:33], v[58:65], v[70:73], v227, v227 op_sel_hi:[0,0,0]
	s_setprio 0
	s_setprio 1
	v_mfma_scale_f32_16x16x128_f8f6f4 v[122:125], v[2:9], v[34:41], v[122:125], v227, v227 op_sel_hi:[0,0,0]
	v_mfma_scale_f32_16x16x128_f8f6f4 v[114:117], v[10:17], v[34:41], v[114:117], v227, v227 op_sel_hi:[0,0,0]
	v_mfma_scale_f32_16x16x128_f8f6f4 v[106:109], v[2:9], v[42:49], v[106:109], v227, v227 op_sel_hi:[0,0,0]
	v_mfma_scale_f32_16x16x128_f8f6f4 v[98:101], v[10:17], v[42:49], v[98:101], v227, v227 op_sel_hi:[0,0,0]
	v_mfma_scale_f32_16x16x128_f8f6f4 v[90:93], v[2:9], v[50:57], v[90:93], v227, v227 op_sel_hi:[0,0,0]
	v_mfma_scale_f32_16x16x128_f8f6f4 v[82:85], v[10:17], v[50:57], v[82:85], v227, v227 op_sel_hi:[0,0,0]
	v_mfma_scale_f32_16x16x128_f8f6f4 v[74:77], v[2:9], v[58:65], v[74:77], v227, v227 op_sel_hi:[0,0,0]
	v_mfma_scale_f32_16x16x128_f8f6f4 v[66:69], v[10:17], v[58:65], v[66:69], v227, v227 op_sel_hi:[0,0,0]
; #define G8_STAGE(bufoff, gbase, voff) do { _Pragma("unroll") for (int _i = 0; _i < 2; ++_i) \
;         __builtin_amdgcn_global_load_lds((const unsigned*)((const char*)(gbase) + (voff)[_i]), (LAS unsigned*)(lds + (bufoff) + ldsw + _i * 8192), 16, 0, 0); } while (0)
; #define G8_LDA(dst, b, h) do { _Pragma("unroll") for (int m = 0; m < 4; ++m) _Pragma("unroll") for (int k = 0; k < 2; ++k) dst[m][k] = *(const LAS bf16x8*)(lds + G8_SA(b, h) + aoff + m * 2048 + k * 1024); } while (0)
; #define G8_LDB(dst, b, h) do { _Pragma("unroll") for (int n = 0; n < 2; ++n) _Pragma("unroll") for (int k = 0; k < 2; ++k) dst[n][k] = *(const LAS bf16x8*)(lds + G8_SB(b, h) + boff + n * 2048 + k * 1024); } while (0)
; #define G8_WAIT_V(n) asm volatile("s_waitcnt vmcnt(" #n ")" ::: "memory")
; #define G8_WAIT_L(n) asm volatile("s_waitcnt lgkmcnt(" #n ")" ::: "memory")
; #define G8_BAR __builtin_amdgcn_s_barrier()
; #define G8_SCHED __builtin_amdgcn_sched_barrier(0)
; template <class Epi, class Sched, int NT, bool F8 = false>
; __device__ __forceinline__ void gemm_phase(LAS unsigned char* lds, const Sched& S, const Epi& E) {
;     ...
;             G8_WAIT_VF(t, ui); G8_WAIT_L(0); G8_BAR; G8_MMA(1, 0, At, B0); G8_MMA(1, 1, At, B1); G8_BAR; G8_SCHED;
;             G8_LDB(B0, 1, 0); G8_LDB(B1, 1, 1); G8_SCHED; G8_LDA(At, 1, 0); G8_STAGE(G8_SA(0, 1), a2, cur.vA1);
;             G8_WAIT_V(8); G8_WAIT_L(0); G8_BAR; G8_MMA(0, 0, At, B0); G8_MMA(0, 1, At, B1); G8_BAR; G8_SCHED;
;             G8_LDA(At, 1, 1); G8_STAGE(G8_SB(1, 0), b3, voffB); G8_STAGE(G8_SB(1, 1), b3, voffB1); G8_STAGE(G8_SA(1, 0), a3, cur.vA0);
;             G8_WAIT_V(8); G8_WAIT_L(0); G8_BAR; G8_MMA(1, 0, At, B0); G8_MMA(1, 1, At, B1); G8_BAR; G8_SCHED;
;         }
.Lcz_p81r:
	s_setprio 0
	s_barrier
	v_add_u32_e32 v14, s50, v221
	v_add_u32_e32 v30, s51, v221
	ds_read_b128 v[2:5], v14
	ds_read_b128 v[6:9], v14 offset:1024
	ds_read_b128 v[10:13], v14 offset:2048
	ds_read_b128 v[14:17], v14 offset:3072
	ds_read_b128 v[18:21], v30
	ds_read_b128 v[22:25], v30 offset:1024
	ds_read_b128 v[26:29], v30 offset:2048
	ds_read_b128 v[30:33], v30 offset:3072
	s_mov_b32 m0, s45
	v_lshl_add_u64 v[216:217], s[30:31], 0, v[216:217]
	ds_read_b128 v[34:37], v226 offset:32768
	ds_read_b128 v[38:41], v226 offset:33792
	ds_read_b128 v[42:45], v226 offset:34816
	ds_read_b128 v[46:49], v226 offset:35840
	ds_read_b128 v[50:53], v226 offset:36864
	ds_read_b128 v[54:57], v226 offset:37888
	ds_read_b128 v[58:61], v226 offset:38912
	ds_read_b128 v[62:65], v226 offset:39936
	global_load_lds_dwordx4 v[216:217], off
	v_lshl_add_u64 v[214:215], s[30:31], 0, v[214:215]
	s_mov_b32 m0, s47
	s_nop 0
	global_load_lds_dwordx4 v[214:215], off
	s_waitcnt vmcnt(8)
	s_waitcnt lgkmcnt(0)
	s_barrier
	s_setprio 1
	s_waitcnt lgkmcnt(0)
	v_mfma_scale_f32_16x16x128_f8f6f4 v[190:193], v[2:9], v[34:41], v[190:193], v227, v227 op_sel_hi:[0,0,0]
	v_mfma_scale_f32_16x16x128_f8f6f4 v[182:185], v[10:17], v[34:41], v[182:185], v227, v227 op_sel_hi:[0,0,0]
	v_mfma_scale_f32_16x16x128_f8f6f4 v[174:177], v[2:9], v[42:49], v[174:177], v227, v227 op_sel_hi:[0,0,0]
	v_mfma_scale_f32_16x16x128_f8f6f4 v[166:169], v[10:17], v[42:49], v[166:169], v227, v227 op_sel_hi:[0,0,0]
	v_mfma_scale_f32_16x16x128_f8f6f4 v[158:161], v[2:9], v[50:57], v[158:161], v227, v227 op_sel_hi:[0,0,0]
	v_mfma_scale_f32_16x16x128_f8f6f4 v[150:153], v[10:17], v[50:57], v[150:153], v227, v227 op_sel_hi:[0,0,0]
	v_mfma_scale_f32_16x16x128_f8f6f4 v[142:145], v[2:9], v[58:65], v[142:145], v227, v227 op_sel_hi:[0,0,0]
	v_mfma_scale_f32_16x16x128_f8f6f4 v[134:137], v[10:17], v[58:65], v[134:137], v227, v227 op_sel_hi:[0,0,0]
	s_setprio 0
	s_setprio 1
	v_mfma_scale_f32_16x16x128_f8f6f4 v[186:189], v[18:25], v[34:41], v[186:189], v227, v227 op_sel_hi:[0,0,0]
	v_mfma_scale_f32_16x16x128_f8f6f4 v[178:181], v[26:33], v[34:41], v[178:181], v227, v227 op_sel_hi:[0,0,0]
	v_mfma_scale_f32_16x16x128_f8f6f4 v[170:173], v[18:25], v[42:49], v[170:173], v227, v227 op_sel_hi:[0,0,0]
	v_mfma_scale_f32_16x16x128_f8f6f4 v[162:165], v[26:33], v[42:49], v[162:165], v227, v227 op_sel_hi:[0,0,0]
	v_mfma_scale_f32_16x16x128_f8f6f4 v[154:157], v[18:25], v[50:57], v[154:157], v227, v227 op_sel_hi:[0,0,0]
	v_mfma_scale_f32_16x16x128_f8f6f4 v[146:149], v[26:33], v[50:57], v[146:149], v227, v227 op_sel_hi:[0,0,0]
	v_mfma_scale_f32_16x16x128_f8f6f4 v[138:141], v[18:25], v[58:65], v[138:141], v227, v227 op_sel_hi:[0,0,0]
	v_mfma_scale_f32_16x16x128_f8f6f4 v[130:133], v[26:33], v[58:65], v[130:133], v227, v227 op_sel_hi:[0,0,0]
	s_setprio 0
	s_barrier
	s_add_i32 s30, s50, s25
	v_lshl_add_u64 v[214:215], v[232:233], 0, s[2:3]
	s_mov_b32 m0, s30
	ds_read_b128 v[34:37], v226 offset:49152
	ds_read_b128 v[38:41], v226 offset:50176
	ds_read_b128 v[42:45], v226 offset:51200
	ds_read_b128 v[46:49], v226 offset:52224
	ds_read_b128 v[50:53], v226 offset:53248
	ds_read_b128 v[54:57], v226 offset:54272
	ds_read_b128 v[58:61], v226 offset:55296
	ds_read_b128 v[62:65], v226 offset:56320
	global_load_lds_dwordx4 v[214:215], off
	v_lshl_add_u64 v[214:215], v[234:235], 0, s[2:3]
	s_add_i32 m0, s30, 0x2000
	s_add_i32 s30, s51, s25
	global_load_lds_dwordx4 v[214:215], off
	v_lshl_add_u64 v[214:215], s[28:29], 0, v[198:199]
	s_mov_b32 m0, s30
	s_nop 0
	global_load_lds_dwordx4 v[214:215], off
	v_lshl_add_u64 v[214:215], s[28:29], 0, v[202:203]
	s_add_i32 m0, s30, 0x2000
	s_nop 0
	global_load_lds_dwordx4 v[214:215], off
	v_lshl_add_u64 v[214:215], v[236:237], 0, s[2:3]
	s_mov_b32 m0, s48
	s_nop 0
	global_load_lds_dwordx4 v[214:215], off
	v_lshl_add_u64 v[214:215], v[238:239], 0, s[2:3]
	s_mov_b32 m0, s49
	s_nop 0
	global_load_lds_dwordx4 v[214:215], off
	s_waitcnt vmcnt(8)
	s_waitcnt lgkmcnt(0)
	s_barrier
	s_setprio 1
	s_waitcnt lgkmcnt(0)
	v_mfma_scale_f32_16x16x128_f8f6f4 v[126:129], v[2:9], v[34:41], v[126:129], v227, v227 op_sel_hi:[0,0,0]
	v_mfma_scale_f32_16x16x128_f8f6f4 v[118:121], v[10:17], v[34:41], v[118:121], v227, v227 op_sel_hi:[0,0,0]
	v_mfma_scale_f32_16x16x128_f8f6f4 v[110:113], v[2:9], v[42:49], v[110:113], v227, v227 op_sel_hi:[0,0,0]
	v_mfma_scale_f32_16x16x128_f8f6f4 v[102:105], v[10:17], v[42:49], v[102:105], v227, v227 op_sel_hi:[0,0,0]
	v_mfma_scale_f32_16x16x128_f8f6f4 v[94:97], v[2:9], v[50:57], v[94:97], v227, v227 op_sel_hi:[0,0,0]
	v_mfma_scale_f32_16x16x128_f8f6f4 v[86:89], v[10:17], v[50:57], v[86:89], v227, v227 op_sel_hi:[0,0,0]
	v_mfma_scale_f32_16x16x128_f8f6f4 v[78:81], v[2:9], v[58:65], v[78:81], v227, v227 op_sel_hi:[0,0,0]
	v_mfma_scale_f32_16x16x128_f8f6f4 v[70:73], v[10:17], v[58:65], v[70:73], v227, v227 op_sel_hi:[0,0,0]
	s_setprio 0
	s_setprio 1
	v_mfma_scale_f32_16x16x128_f8f6f4 v[122:125], v[18:25], v[34:41], v[122:125], v227, v227 op_sel_hi:[0,0,0]
	v_mfma_scale_f32_16x16x128_f8f6f4 v[114:117], v[26:33], v[34:41], v[114:117], v227, v227 op_sel_hi:[0,0,0]
	v_mfma_scale_f32_16x16x128_f8f6f4 v[106:109], v[18:25], v[42:49], v[106:109], v227, v227 op_sel_hi:[0,0,0]
	v_mfma_scale_f32_16x16x128_f8f6f4 v[98:101], v[26:33], v[42:49], v[98:101], v227, v227 op_sel_hi:[0,0,0]
	v_mfma_scale_f32_16x16x128_f8f6f4 v[90:93], v[18:25], v[50:57], v[90:93], v227, v227 op_sel_hi:[0,0,0]
	v_mfma_scale_f32_16x16x128_f8f6f4 v[82:85], v[26:33], v[50:57], v[82:85], v227, v227 op_sel_hi:[0,0,0]
	v_mfma_scale_f32_16x16x128_f8f6f4 v[74:77], v[18:25], v[58:65], v[74:77], v227, v227 op_sel_hi:[0,0,0]
	v_mfma_scale_f32_16x16x128_f8f6f4 v[66:69], v[26:33], v[58:65], v[66:69], v227, v227 op_sel_hi:[0,0,0]
	s_setprio 0
	s_barrier
	s_add_u32 s26, s26, 0x100
	s_addc_u32 s27, s27, 0
	s_add_u32 s19, s19, 0x100
	s_addc_u32 s57, s57, 0
	s_cmp_gt_u32 s58, 13
	s_cbranch_scc1 .LBB0_846

.Lcz_p80:
	v_mfma_scale_f32_16x16x128_f8f6f4 v[190:193], v[18:25], v[58:65], 0, v227, v227 op_sel_hi:[0,0,0]
	v_mfma_scale_f32_16x16x128_f8f6f4 v[182:185], v[26:33], v[58:65], 0, v227, v227 op_sel_hi:[0,0,0]
	v_mfma_scale_f32_16x16x128_f8f6f4 v[174:177], v[18:25], v[50:57], 0, v227, v227 op_sel_hi:[0,0,0]
	v_mfma_scale_f32_16x16x128_f8f6f4 v[166:169], v[26:33], v[50:57], 0, v227, v227 op_sel_hi:[0,0,0]
	v_mfma_scale_f32_16x16x128_f8f6f4 v[158:161], v[18:25], v[42:49], 0, v227, v227 op_sel_hi:[0,0,0]
	v_mfma_scale_f32_16x16x128_f8f6f4 v[150:153], v[26:33], v[42:49], 0, v227, v227 op_sel_hi:[0,0,0]
	v_mfma_scale_f32_16x16x128_f8f6f4 v[142:145], v[18:25], v[34:41], 0, v227, v227 op_sel_hi:[0,0,0]
	v_mfma_scale_f32_16x16x128_f8f6f4 v[134:137], v[26:33], v[34:41], 0, v227, v227 op_sel_hi:[0,0,0]
	s_setprio 0
	s_setprio 1
	v_mfma_scale_f32_16x16x128_f8f6f4 v[186:189], v[2:9], v[58:65], 0, v227, v227 op_sel_hi:[0,0,0]
	v_mfma_scale_f32_16x16x128_f8f6f4 v[178:181], v[10:17], v[58:65], 0, v227, v227 op_sel_hi:[0,0,0]
	v_mfma_scale_f32_16x16x128_f8f6f4 v[170:173], v[2:9], v[50:57], 0, v227, v227 op_sel_hi:[0,0,0]
	v_mfma_scale_f32_16x16x128_f8f6f4 v[162:165], v[10:17], v[50:57], 0, v227, v227 op_sel_hi:[0,0,0]
	v_mfma_scale_f32_16x16x128_f8f6f4 v[154:157], v[2:9], v[42:49], 0, v227, v227 op_sel_hi:[0,0,0]
	v_mfma_scale_f32_16x16x128_f8f6f4 v[146:149], v[10:17], v[42:49], 0, v227, v227 op_sel_hi:[0,0,0]
	v_mfma_scale_f32_16x16x128_f8f6f4 v[138:141], v[2:9], v[34:41], 0, v227, v227 op_sel_hi:[0,0,0]
	v_mfma_scale_f32_16x16x128_f8f6f4 v[130:133], v[10:17], v[34:41], 0, v227, v227 op_sel_hi:[0,0,0]
	s_branch .Lcz_p80r
.Lcz_p81:
	v_mfma_scale_f32_16x16x128_f8f6f4 v[126:129], v[18:25], v[34:41], 0, v227, v227 op_sel_hi:[0,0,0]
	v_mfma_scale_f32_16x16x128_f8f6f4 v[118:121], v[26:33], v[34:41], 0, v227, v227 op_sel_hi:[0,0,0]
	v_mfma_scale_f32_16x16x128_f8f6f4 v[110:113], v[18:25], v[42:49], 0, v227, v227 op_sel_hi:[0,0,0]
	v_mfma_scale_f32_16x16x128_f8f6f4 v[102:105], v[26:33], v[42:49], 0, v227, v227 op_sel_hi:[0,0,0]
	v_mfma_scale_f32_16x16x128_f8f6f4 v[94:97], v[18:25], v[50:57], 0, v227, v227 op_sel_hi:[0,0,0]
	v_mfma_scale_f32_16x16x128_f8f6f4 v[86:89], v[26:33], v[50:57], 0, v227, v227 op_sel_hi:[0,0,0]
	v_mfma_scale_f32_16x16x128_f8f6f4 v[78:81], v[18:25], v[58:65], 0, v227, v227 op_sel_hi:[0,0,0]
	v_mfma_scale_f32_16x16x128_f8f6f4 v[70:73], v[26:33], v[58:65], 0, v227, v227 op_sel_hi:[0,0,0]
	s_setprio 0
	s_setprio 1
	v_mfma_scale_f32_16x16x128_f8f6f4 v[122:125], v[2:9], v[34:41], 0, v227, v227 op_sel_hi:[0,0,0]
	v_mfma_scale_f32_16x16x128_f8f6f4 v[114:117], v[10:17], v[34:41], 0, v227, v227 op_sel_hi:[0,0,0]
	v_mfma_scale_f32_16x16x128_f8f6f4 v[106:109], v[2:9], v[42:49], 0, v227, v227 op_sel_hi:[0,0,0]
	v_mfma_scale_f32_16x16x128_f8f6f4 v[98:101], v[10:17], v[42:49], 0, v227, v227 op_sel_hi:[0,0,0]
	v_mfma_scale_f32_16x16x128_f8f6f4 v[90:93], v[2:9], v[50:57], 0, v227, v227 op_sel_hi:[0,0,0]
	v_mfma_scale_f32_16x16x128_f8f6f4 v[82:85], v[10:17], v[50:57], 0, v227, v227 op_sel_hi:[0,0,0]
	v_mfma_scale_f32_16x16x128_f8f6f4 v[74:77], v[2:9], v[58:65], 0, v227, v227 op_sel_hi:[0,0,0]
	v_mfma_scale_f32_16x16x128_f8f6f4 v[66:69], v[10:17], v[58:65], 0, v227, v227 op_sel_hi:[0,0,0]
	s_branch .Lcz_p81r

; #define G8_BAR __builtin_amdgcn_s_barrier()
; template <class Epi, class Sched, int NT, bool F8 = false>
; __device__ __forceinline__ void gemm_phase(LAS unsigned char* lds, const Sched& S, const Epi& E) {
;     ...
;         if (!has_next) break;
; #pragma unroll
;         for (int a = 0; a < 2; ++a)
; #pragma unroll
;             for (int b = 0; b < 2; ++b)
; #pragma unroll
;                 for (int m = 0; m < 4; ++m)
; #pragma unroll
;                     for (int n = 0; n < 2; ++n) acc[a][b][m][n] = (f32x4){0.f, 0.f, 0.f, 0.f};
;         cur = nxt; cA = nA; cB = nB; ++ui;
;         if (wr == 1) G8_BAR;
.LBB0_943:
	v_mov_b32_e32 v66, 0
	v_mov_b32_e32 v205, v203
	v_mov_b32_e32 v207, v203
	s_mov_b32 s13, 0
	s_mov_b64 s[30:31], -1
	s_mov_b64 s[28:29], 0
	s_branch .LBB0_946

; #define G8_STAGE(bufoff, gbase, voff) do { _Pragma("unroll") for (int _i = 0; _i < 2; ++_i) \
;         __builtin_amdgcn_global_load_lds((const unsigned*)((const char*)(gbase) + (voff)[_i]), (LAS unsigned*)(lds + (bufoff) + ldsw + _i * 8192), 16, 0, 0); } while (0)
; #define G8_LDA(dst, b, h) do { _Pragma("unroll") for (int m = 0; m < 4; ++m) _Pragma("unroll") for (int k = 0; k < 2; ++k) dst[m][k] = *(const LAS bf16x8*)(lds + G8_SA(b, h) + aoff + m * 2048 + k * 1024); } while (0)
; #define G8_WAIT_L(n) asm volatile("s_waitcnt lgkmcnt(" #n ")" ::: "memory")
; #define G8_BAR __builtin_amdgcn_s_barrier()
; #define G8_SCHED __builtin_amdgcn_sched_barrier(0)
; template <class Epi, class Sched, int NT, bool F8 = false>
; __device__ __forceinline__ void gemm_phase(LAS unsigned char* lds, const Sched& S, const Epi& E) {
;     ...
;             G8_WAIT_VF(t, ui); G8_WAIT_L(0); G8_BAR; G8_MMA(0, 0, At, B0); G8_MMA(0, 1, At, B1); G8_BAR; G8_SCHED;
;             G8_LDA(At, 0, 1); G8_STAGE(G8_SB(0, 0), b2, voffB); G8_STAGE(G8_SB(0, 1), b2, voffB1); G8_STAGE(G8_SA(0, 0), a2, cur.vA0);
.LwAe:
	s_waitcnt lgkmcnt(0)
	s_barrier
	s_setprio 1
	s_waitcnt lgkmcnt(0)
	s_cmp_eq_u32 s13, 0
	s_cbranch_scc1 .Lcz_p90
	v_mfma_scale_f32_16x16x128_f8f6f4 v[190:193], v[18:25], v[58:65], v[190:193], v227, v227 op_sel_hi:[0,0,0]
	v_mfma_scale_f32_16x16x128_f8f6f4 v[186:189], v[26:33], v[58:65], v[186:189], v227, v227 op_sel_hi:[0,0,0]
	v_mfma_scale_f32_16x16x128_f8f6f4 v[178:181], v[18:25], v[50:57], v[178:181], v227, v227 op_sel_hi:[0,0,0]
	v_mfma_scale_f32_16x16x128_f8f6f4 v[170:173], v[26:33], v[50:57], v[170:173], v227, v227 op_sel_hi:[0,0,0]
	v_mfma_scale_f32_16x16x128_f8f6f4 v[162:165], v[18:25], v[42:49], v[162:165], v227, v227 op_sel_hi:[0,0,0]
	v_mfma_scale_f32_16x16x128_f8f6f4 v[154:157], v[26:33], v[42:49], v[154:157], v227, v227 op_sel_hi:[0,0,0]
	v_mfma_scale_f32_16x16x128_f8f6f4 v[146:149], v[18:25], v[34:41], v[146:149], v227, v227 op_sel_hi:[0,0,0]
	v_mfma_scale_f32_16x16x128_f8f6f4 v[138:141], v[26:33], v[34:41], v[138:141], v227, v227 op_sel_hi:[0,0,0]
	s_setprio 0
	s_setprio 1
	v_mfma_scale_f32_16x16x128_f8f6f4 v[182:185], v[2:9], v[58:65], v[182:185], v227, v227 op_sel_hi:[0,0,0]
	v_mfma_scale_f32_16x16x128_f8f6f4 v[174:177], v[10:17], v[58:65], v[174:177], v227, v227 op_sel_hi:[0,0,0]
	v_mfma_scale_f32_16x16x128_f8f6f4 v[166:169], v[2:9], v[50:57], v[166:169], v227, v227 op_sel_hi:[0,0,0]
	v_mfma_scale_f32_16x16x128_f8f6f4 v[158:161], v[10:17], v[50:57], v[158:161], v227, v227 op_sel_hi:[0,0,0]
	v_mfma_scale_f32_16x16x128_f8f6f4 v[150:153], v[2:9], v[42:49], v[150:153], v227, v227 op_sel_hi:[0,0,0]
	v_mfma_scale_f32_16x16x128_f8f6f4 v[142:145], v[10:17], v[42:49], v[142:145], v227, v227 op_sel_hi:[0,0,0]
	v_mfma_scale_f32_16x16x128_f8f6f4 v[134:137], v[2:9], v[34:41], v[134:137], v227, v227 op_sel_hi:[0,0,0]
	v_mfma_scale_f32_16x16x128_f8f6f4 v[130:133], v[10:17], v[34:41], v[130:133], v227, v227 op_sel_hi:[0,0,0]
.Lcz_p90r:
	s_setprio 0
	s_barrier
	s_mov_b32 m0, s42
	v_lshl_add_u64 v[232:233], s[34:35], 0, v[200:201]
	ds_read_b128 v[34:37], v226 offset:16384
	ds_read_b128 v[38:41], v226 offset:17408
	ds_read_b128 v[42:45], v226 offset:18432
	ds_read_b128 v[46:49], v226 offset:19456
	ds_read_b128 v[50:53], v226 offset:20480
	ds_read_b128 v[54:57], v226 offset:21504
	ds_read_b128 v[58:61], v226 offset:22528
	ds_read_b128 v[62:65], v226 offset:23552
	global_load_lds_dwordx4 v[232:233], off
	v_lshl_add_u64 v[234:235], s[34:35], 0, v[196:197]
	s_mov_b32 m0, s43
	v_lshl_add_u64 v[236:237], s[34:35], 0, v[198:199]
	global_load_lds_dwordx4 v[234:235], off
	s_mov_b32 m0, s44
	v_mov_b32_e32 v211, v203
	global_load_lds_dwordx4 v[236:237], off
	v_lshl_add_u64 v[236:237], s[34:35], 0, v[194:195]
	s_mov_b32 m0, s45
	v_mov_b32_e32 v213, v203
	global_load_lds_dwordx4 v[236:237], off
	s_mov_b32 m0, s21
	v_lshl_add_u64 v[236:237], s[30:31], 0, v[210:211]
	global_load_lds_dwordx4 v210, s[30:31]
	s_mov_b32 m0, s46
	v_lshl_add_u64 v[238:239], s[30:31], 0, v[212:213]
	global_load_lds_dwordx4 v212, s[30:31]
	s_cmp_eq_u32 s100, 0
	s_cbranch_scc1 .LdfB
	v_add_u32_e32 v252, s98, v221
	v_lshlrev_b32_e32 v252, 11, v252
	v_add3_u32 v252, v252, s99, v223
	v_add_u32_e32 v252, 0x48000, v252
	global_store_dwordx4 v252, v[240:243], s[8:9]

; #define G8_STAGE(bufoff, gbase, voff) do { _Pragma("unroll") for (int _i = 0; _i < 2; ++_i) \
;         __builtin_amdgcn_global_load_lds((const unsigned*)((const char*)(gbase) + (voff)[_i]), (LAS unsigned*)(lds + (bufoff) + ldsw + _i * 8192), 16, 0, 0); } while (0)
; #define G8_LDA(dst, b, h) do { _Pragma("unroll") for (int m = 0; m < 4; ++m) _Pragma("unroll") for (int k = 0; k < 2; ++k) dst[m][k] = *(const LAS bf16x8*)(lds + G8_SA(b, h) + aoff + m * 2048 + k * 1024); } while (0)
; #define G8_LDB(dst, b, h) do { _Pragma("unroll") for (int n = 0; n < 2; ++n) _Pragma("unroll") for (int k = 0; k < 2; ++k) dst[n][k] = *(const LAS bf16x8*)(lds + G8_SB(b, h) + boff + n * 2048 + k * 1024); } while (0)
; #define G8_WAIT_L(n) asm volatile("s_waitcnt lgkmcnt(" #n ")" ::: "memory")
; #define G8_BAR __builtin_amdgcn_s_barrier()
; #define G8_SCHED __builtin_amdgcn_sched_barrier(0)
; template <class Epi, class Sched, int NT, bool F8 = false>
; __device__ __forceinline__ void gemm_phase(LAS unsigned char* lds, const Sched& S, const Epi& E) {
;     ...
;             G8_WAIT_VF(t, ui); G8_WAIT_L(0); G8_BAR; G8_MMA(1, 0, At, B0); G8_MMA(1, 1, At, B1); G8_BAR; G8_SCHED;
;             G8_LDB(B0, 1, 0); G8_LDB(B1, 1, 1); G8_SCHED; G8_LDA(At, 1, 0); G8_STAGE(G8_SA(0, 1), a2, cur.vA1);
.LwBe:
	s_waitcnt lgkmcnt(0)
	s_barrier
	s_setprio 1
	s_waitcnt lgkmcnt(0)
	s_cmp_eq_u32 s13, 0
	s_cbranch_scc1 .Lcz_p91
	v_mfma_scale_f32_16x16x128_f8f6f4 v[126:129], v[18:25], v[34:41], v[126:129], v227, v227 op_sel_hi:[0,0,0]
	v_mfma_scale_f32_16x16x128_f8f6f4 v[122:125], v[26:33], v[34:41], v[122:125], v227, v227 op_sel_hi:[0,0,0]
	v_mfma_scale_f32_16x16x128_f8f6f4 v[114:117], v[18:25], v[42:49], v[114:117], v227, v227 op_sel_hi:[0,0,0]
	v_mfma_scale_f32_16x16x128_f8f6f4 v[106:109], v[26:33], v[42:49], v[106:109], v227, v227 op_sel_hi:[0,0,0]
	v_mfma_scale_f32_16x16x128_f8f6f4 v[98:101], v[18:25], v[50:57], v[98:101], v227, v227 op_sel_hi:[0,0,0]
	v_mfma_scale_f32_16x16x128_f8f6f4 v[90:93], v[26:33], v[50:57], v[90:93], v227, v227 op_sel_hi:[0,0,0]
	v_mfma_scale_f32_16x16x128_f8f6f4 v[82:85], v[18:25], v[58:65], v[82:85], v227, v227 op_sel_hi:[0,0,0]
	v_mfma_scale_f32_16x16x128_f8f6f4 v[74:77], v[26:33], v[58:65], v[74:77], v227, v227 op_sel_hi:[0,0,0]
	s_setprio 0
	s_setprio 1
	v_mfma_scale_f32_16x16x128_f8f6f4 v[118:121], v[2:9], v[34:41], v[118:121], v227, v227 op_sel_hi:[0,0,0]
	v_mfma_scale_f32_16x16x128_f8f6f4 v[110:113], v[10:17], v[34:41], v[110:113], v227, v227 op_sel_hi:[0,0,0]
	v_mfma_scale_f32_16x16x128_f8f6f4 v[102:105], v[2:9], v[42:49], v[102:105], v227, v227 op_sel_hi:[0,0,0]
	v_mfma_scale_f32_16x16x128_f8f6f4 v[94:97], v[10:17], v[42:49], v[94:97], v227, v227 op_sel_hi:[0,0,0]
	v_mfma_scale_f32_16x16x128_f8f6f4 v[86:89], v[2:9], v[50:57], v[86:89], v227, v227 op_sel_hi:[0,0,0]
	v_mfma_scale_f32_16x16x128_f8f6f4 v[78:81], v[10:17], v[50:57], v[78:81], v227, v227 op_sel_hi:[0,0,0]
	v_mfma_scale_f32_16x16x128_f8f6f4 v[70:73], v[2:9], v[58:65], v[70:73], v227, v227 op_sel_hi:[0,0,0]
	v_mfma_scale_f32_16x16x128_f8f6f4 v[66:69], v[10:17], v[58:65], v[66:69], v227, v227 op_sel_hi:[0,0,0]
.Lcz_p91r:
	s_setprio 0
	s_barrier
	v_add_u32_e32 v14, s56, v222
	v_add_u32_e32 v30, s57, v222
	ds_read_b128 v[2:5], v14
	ds_read_b128 v[6:9], v14 offset:1024
	ds_read_b128 v[10:13], v14 offset:2048
	ds_read_b128 v[14:17], v14 offset:3072
	ds_read_b128 v[18:21], v30
	ds_read_b128 v[22:25], v30 offset:1024
	ds_read_b128 v[26:29], v30 offset:2048
	ds_read_b128 v[30:33], v30 offset:3072
	s_mov_b32 m0, s47
	v_lshl_add_u64 v[216:217], s[30:31], 0, v[216:217]
	ds_read_b128 v[34:37], v226 offset:32768
	ds_read_b128 v[38:41], v226 offset:33792
	ds_read_b128 v[42:45], v226 offset:34816
	ds_read_b128 v[46:49], v226 offset:35840
	ds_read_b128 v[50:53], v226 offset:36864
	ds_read_b128 v[54:57], v226 offset:37888
	ds_read_b128 v[58:61], v226 offset:38912
	ds_read_b128 v[62:65], v226 offset:39936
	global_load_lds_dwordx4 v[216:217], off
	v_lshl_add_u64 v[214:215], s[30:31], 0, v[214:215]
	s_mov_b32 m0, s48
	s_nop 0
	global_load_lds_dwordx4 v[214:215], off
	s_cmp_eq_u32 s100, 0
	s_cbranch_scc1 .LdfC
	v_add_u32_e32 v252, s98, v221
	v_lshlrev_b32_e32 v252, 11, v252
	v_add3_u32 v252, v252, s99, v223
	v_add_u32_e32 v252, 0x50000, v252
	global_store_dwordx4 v252, v[244:247], s[8:9]

.Lcz_p90:
	v_mfma_scale_f32_16x16x128_f8f6f4 v[190:193], v[18:25], v[58:65], 0, v227, v227 op_sel_hi:[0,0,0]
	v_mfma_scale_f32_16x16x128_f8f6f4 v[186:189], v[26:33], v[58:65], 0, v227, v227 op_sel_hi:[0,0,0]
	v_mfma_scale_f32_16x16x128_f8f6f4 v[178:181], v[18:25], v[50:57], 0, v227, v227 op_sel_hi:[0,0,0]
	v_mfma_scale_f32_16x16x128_f8f6f4 v[170:173], v[26:33], v[50:57], 0, v227, v227 op_sel_hi:[0,0,0]
	v_mfma_scale_f32_16x16x128_f8f6f4 v[162:165], v[18:25], v[42:49], 0, v227, v227 op_sel_hi:[0,0,0]
	v_mfma_scale_f32_16x16x128_f8f6f4 v[154:157], v[26:33], v[42:49], 0, v227, v227 op_sel_hi:[0,0,0]
	v_mfma_scale_f32_16x16x128_f8f6f4 v[146:149], v[18:25], v[34:41], 0, v227, v227 op_sel_hi:[0,0,0]
	v_mfma_scale_f32_16x16x128_f8f6f4 v[138:141], v[26:33], v[34:41], 0, v227, v227 op_sel_hi:[0,0,0]
	s_setprio 0
	s_setprio 1
	v_mfma_scale_f32_16x16x128_f8f6f4 v[182:185], v[2:9], v[58:65], 0, v227, v227 op_sel_hi:[0,0,0]
	v_mfma_scale_f32_16x16x128_f8f6f4 v[174:177], v[10:17], v[58:65], 0, v227, v227 op_sel_hi:[0,0,0]
	v_mfma_scale_f32_16x16x128_f8f6f4 v[166:169], v[2:9], v[50:57], 0, v227, v227 op_sel_hi:[0,0,0]
	v_mfma_scale_f32_16x16x128_f8f6f4 v[158:161], v[10:17], v[50:57], 0, v227, v227 op_sel_hi:[0,0,0]
	v_mfma_scale_f32_16x16x128_f8f6f4 v[150:153], v[2:9], v[42:49], 0, v227, v227 op_sel_hi:[0,0,0]
	v_mfma_scale_f32_16x16x128_f8f6f4 v[142:145], v[10:17], v[42:49], 0, v227, v227 op_sel_hi:[0,0,0]
	v_mfma_scale_f32_16x16x128_f8f6f4 v[134:137], v[2:9], v[34:41], 0, v227, v227 op_sel_hi:[0,0,0]
	v_mfma_scale_f32_16x16x128_f8f6f4 v[130:133], v[10:17], v[34:41], 0, v227, v227 op_sel_hi:[0,0,0]
	s_branch .Lcz_p90r
.Lcz_p91:
	v_mfma_scale_f32_16x16x128_f8f6f4 v[126:129], v[18:25], v[34:41], 0, v227, v227 op_sel_hi:[0,0,0]
	v_mfma_scale_f32_16x16x128_f8f6f4 v[122:125], v[26:33], v[34:41], 0, v227, v227 op_sel_hi:[0,0,0]
	v_mfma_scale_f32_16x16x128_f8f6f4 v[114:117], v[18:25], v[42:49], 0, v227, v227 op_sel_hi:[0,0,0]
	v_mfma_scale_f32_16x16x128_f8f6f4 v[106:109], v[26:33], v[42:49], 0, v227, v227 op_sel_hi:[0,0,0]
	v_mfma_scale_f32_16x16x128_f8f6f4 v[98:101], v[18:25], v[50:57], 0, v227, v227 op_sel_hi:[0,0,0]
	v_mfma_scale_f32_16x16x128_f8f6f4 v[90:93], v[26:33], v[50:57], 0, v227, v227 op_sel_hi:[0,0,0]
	v_mfma_scale_f32_16x16x128_f8f6f4 v[82:85], v[18:25], v[58:65], 0, v227, v227 op_sel_hi:[0,0,0]
	v_mfma_scale_f32_16x16x128_f8f6f4 v[74:77], v[26:33], v[58:65], 0, v227, v227 op_sel_hi:[0,0,0]
	s_setprio 0
	s_setprio 1
	v_mfma_scale_f32_16x16x128_f8f6f4 v[118:121], v[2:9], v[34:41], 0, v227, v227 op_sel_hi:[0,0,0]
	v_mfma_scale_f32_16x16x128_f8f6f4 v[110:113], v[10:17], v[34:41], 0, v227, v227 op_sel_hi:[0,0,0]
	v_mfma_scale_f32_16x16x128_f8f6f4 v[102:105], v[2:9], v[42:49], 0, v227, v227 op_sel_hi:[0,0,0]
	v_mfma_scale_f32_16x16x128_f8f6f4 v[94:97], v[10:17], v[42:49], 0, v227, v227 op_sel_hi:[0,0,0]
	v_mfma_scale_f32_16x16x128_f8f6f4 v[86:89], v[2:9], v[50:57], 0, v227, v227 op_sel_hi:[0,0,0]
	v_mfma_scale_f32_16x16x128_f8f6f4 v[78:81], v[10:17], v[50:57], 0, v227, v227 op_sel_hi:[0,0,0]
	v_mfma_scale_f32_16x16x128_f8f6f4 v[70:73], v[2:9], v[58:65], 0, v227, v227 op_sel_hi:[0,0,0]
	v_mfma_scale_f32_16x16x128_f8f6f4 v[66:69], v[10:17], v[58:65], 0, v227, v227 op_sel_hi:[0,0,0]
	s_branch .Lcz_p91r
